# scan loop: S*=gl as plain v_mul (no packed f32 beside MFMAs), fillers rebalanced over the 32 MFMA gaps
# speedup vs baseline: 1.0278x; 1.0027x over previous
; DI float bflo(unsigned u) { return __uint_as_float(u << 16); }
; DI float bfhi(unsigned u) { return __uint_as_float(u & 0xffff0000u); }
; DI bf16x8 packS(const f32x16& x, int s) { return pack8(x[8 * s], x[8 * s + 1], x[8 * s + 2], x[8 * s + 3], x[8 * s + 4], x[8 * s + 5], x[8 * s + 6], x[8 * s + 7]); }
; #define SCAN_RDW(F, mh) do { _Pragma("unroll") for (int k = 0; k < 8; ++k) { const int i2 = k >> 2, m = 2 * (mh) + ((k >> 1) & 1), sx = k & 1; F[k] = *(const bf16x8*)(lw + ((i2 * 4 + m) * 2 + sx) * 1024); } } while (0)
; DI void gdn_scan_seq(const Params& p, int bh16, char* ldsf) {
;     ...
;     for (int m = 0; m < 4; ++m) { Sb[m][0] = packS(S[m], 0); Sb[m][1] = packS(S[m], 1); *(bf16x8*)(sco + (m * 2 + 0) * 1024) = Sb[m][0]; *(bf16x8*)(sco + (m * 2 + 1) * 1024) = Sb[m][1]; }
;     __builtin_amdgcn_sched_barrier(0);
;     if (c + 2 < 128) { const int s2 = sl >= 1 ? sl - 1 : 2; SCAN_ISSUE(c + 2, s2); }
;     const char* base = ldsf + sl * 49152;
;     const char* lw = base + lane * 16; const char* lk = lw + 16384; const char* lu = base + 32768 + wv * 4096 + lane * 16;
;     const float gl = glt[c];
;     f32x16 vn[2];
; #pragma unroll
;     for (int i2 = 0; i2 < 2; ++i2) {
;       const u32x4 ua = *(const u32x4*)(lu + (2 * i2) * 1024), ub = *(const u32x4*)(lu + (2 * i2 + 1) * 1024);
; #pragma unroll
;       for (int e = 0; e < 4; ++e) { vn[i2][2 * e] = bflo(ua[e]); vn[i2][2 * e + 1] = bfhi(ua[e]); vn[i2][8 + 2 * e] = bflo(ub[e]); vn[i2][8 + 2 * e + 1] = bfhi(ub[e]); }
;     }
;     bf16x8 fa[8], fb[8];
;     ...
;     SCAN_RDW(fa, 0);
;     __builtin_amdgcn_sched_barrier(0);
;     SCAN_RDW(fb, 1);
;     __builtin_amdgcn_sched_barrier(0);
;     SCAN_MMW(fa, 0);
;     __builtin_amdgcn_sched_barrier(0);
;     SCAN_RDK(fa, 0);
;     __builtin_amdgcn_sched_barrier(0);
;     SCAN_MMW(fb, 1);
;     __builtin_amdgcn_sched_barrier(0);
;     SCAN_RDK(fb, 1);
;     __builtin_amdgcn_sched_barrier(0);
;     bf16x8 Vb[2][2];
; #pragma unroll
;     for (int j2 = 0; j2 < 2; ++j2) { Vb[j2][0] = packS(vn[j2], 0); Vb[j2][1] = packS(vn[j2], 1); }
; #pragma unroll
;     for (int m = 0; m < 4; ++m)
; #pragma unroll
;       for (int r = 0; r < 16; ++r) S[m][r] *= gl;
;     SCAN_MMK(fa, 0);
.Lscan_noprog:
	v_add_u32_e32 v131, s3, v130
	v_add_u32_e32 v134, s3, v129
	v_mov_b32_e32 v143, s18
	ds_read_b128 v[72:75], v134 offset:32768
	ds_read_b128 v[76:79], v134 offset:33792
	ds_read_b32 v142, v143
	ds_read_b128 v[148:151], v131 offset:0
	ds_read_b128 v[152:155], v131 offset:1024
	ds_read_b128 v[156:159], v131 offset:2048
	ds_read_b128 v[160:163], v131 offset:3072
	ds_read_b128 v[164:167], v131 offset:4096
	ds_read_b128 v[168:171], v131 offset:5120
	ds_read_b128 v[172:175], v131 offset:6144
	ds_read_b128 v[178:181], v131 offset:7168
	ds_read_b128 v[88:91], v134 offset:34816
	ds_read_b128 v[92:95], v134 offset:35840
	s_waitcnt lgkmcnt(10)
	v_mfma_f32_32x32x16_bf16 v[0:15], v[182:185], v[80:83], v[0:15]
	v_lshlrev_b32_e32 v64, 16, v72
	v_and_b32_e32 v65, 0xffff0000, v72
	v_lshlrev_b32_e32 v66, 16, v73
	v_and_b32_e32 v67, 0xffff0000, v73
	v_mfma_f32_32x32x16_bf16 v[0:15], v[190:193], v[84:87], v[0:15]
	v_lshlrev_b32_e32 v68, 16, v74
	v_and_b32_e32 v69, 0xffff0000, v74
	v_lshlrev_b32_e32 v70, 16, v75
	v_and_b32_e32 v71, 0xffff0000, v75
	v_mfma_f32_32x32x16_bf16 v[16:31], v[194:197], v[80:83], v[16:31]
	v_lshlrev_b32_e32 v72, 16, v76
	v_and_b32_e32 v73, 0xffff0000, v76
	v_lshlrev_b32_e32 v74, 16, v77
	v_and_b32_e32 v75, 0xffff0000, v77
	v_mfma_f32_32x32x16_bf16 v[16:31], v[198:201], v[84:87], v[16:31]
	v_lshlrev_b32_e32 v76, 16, v78
	v_and_b32_e32 v77, 0xffff0000, v78
	v_lshlrev_b32_e32 v78, 16, v79
	v_and_b32_e32 v79, 0xffff0000, v79
	v_mfma_f32_32x32x16_bf16 v[32:47], v[202:205], v[80:83], v[32:47]
	v_cvt_pk_bf16_f32 v96, v0, v1
	v_cvt_pk_bf16_f32 v97, v2, v3
	v_cvt_pk_bf16_f32 v98, v4, v5
	v_cvt_pk_bf16_f32 v99, v6, v7
	v_cvt_pk_bf16_f32 v100, v8, v9
	v_mfma_f32_32x32x16_bf16 v[32:47], v[208:211], v[84:87], v[32:47]
	v_cvt_pk_bf16_f32 v101, v10, v11
	v_cvt_pk_bf16_f32 v102, v12, v13
	v_cvt_pk_bf16_f32 v103, v14, v15
	v_mfma_f32_32x32x16_bf16 v[48:63], v[212:215], v[80:83], v[48:63]
	v_cvt_pk_bf16_f32 v104, v16, v17
	v_cvt_pk_bf16_f32 v105, v18, v19
	v_cvt_pk_bf16_f32 v106, v20, v21
	v_cvt_pk_bf16_f32 v107, v22, v23
	v_cvt_pk_bf16_f32 v108, v24, v25
	v_mfma_f32_32x32x16_bf16 v[48:63], v[216:219], v[84:87], v[48:63]
	v_cvt_pk_bf16_f32 v109, v26, v27
	v_cvt_pk_bf16_f32 v110, v28, v29
	v_cvt_pk_bf16_f32 v111, v30, v31
	s_waitcnt lgkmcnt(0)
	ds_read_b128 v[182:185], v131 offset:8192
	ds_read_b128 v[190:193], v131 offset:9216
	ds_read_b128 v[194:197], v131 offset:10240
	ds_read_b128 v[198:201], v131 offset:11264
	ds_read_b128 v[202:205], v131 offset:12288
	ds_read_b128 v[208:211], v131 offset:13312
	ds_read_b128 v[212:215], v131 offset:14336
	ds_read_b128 v[216:219], v131 offset:15360
	v_mfma_f32_32x32x16_bf16 v[64:79], v[148:151], v[96:99], v[64:79]
	v_cvt_pk_bf16_f32 v112, v32, v33
	v_cvt_pk_bf16_f32 v113, v34, v35
	v_cvt_pk_bf16_f32 v114, v36, v37
	v_cvt_pk_bf16_f32 v115, v38, v39
	v_lshlrev_b32_e32 v80, 16, v88
	v_mfma_f32_32x32x16_bf16 v[64:79], v[152:155], v[100:103], v[64:79]
	v_cvt_pk_bf16_f32 v116, v40, v41
	v_cvt_pk_bf16_f32 v117, v42, v43
	v_cvt_pk_bf16_f32 v118, v44, v45
	v_cvt_pk_bf16_f32 v119, v46, v47
	v_and_b32_e32 v81, 0xffff0000, v88
	v_mfma_f32_32x32x16_bf16 v[64:79], v[156:159], v[104:107], v[64:79]
	v_cvt_pk_bf16_f32 v120, v48, v49
	v_cvt_pk_bf16_f32 v121, v50, v51
	v_cvt_pk_bf16_f32 v122, v52, v53
	v_cvt_pk_bf16_f32 v123, v54, v55
	v_lshlrev_b32_e32 v82, 16, v89
	v_mfma_f32_32x32x16_bf16 v[64:79], v[160:163], v[108:111], v[64:79]
	v_cvt_pk_bf16_f32 v124, v56, v57
	v_cvt_pk_bf16_f32 v125, v58, v59
	v_cvt_pk_bf16_f32 v126, v60, v61
	v_cvt_pk_bf16_f32 v127, v62, v63
	v_and_b32_e32 v83, 0xffff0000, v89
	global_store_dwordx4 v128, v[96:99], s[8:9]
	v_mfma_f32_32x32x16_bf16 v[64:79], v[164:167], v[112:115], v[64:79]
	v_lshlrev_b32_e32 v84, 16, v90
	v_and_b32_e32 v85, 0xffff0000, v90
	v_lshlrev_b32_e32 v86, 16, v91
	v_and_b32_e32 v87, 0xffff0000, v91
	v_lshlrev_b32_e32 v88, 16, v92
	global_store_dwordx4 v128, v[100:103], s[8:9] offset:1024
	v_mfma_f32_32x32x16_bf16 v[64:79], v[168:171], v[116:119], v[64:79]
	v_and_b32_e32 v89, 0xffff0000, v92
	v_lshlrev_b32_e32 v90, 16, v93
	v_and_b32_e32 v91, 0xffff0000, v93
	v_lshlrev_b32_e32 v92, 16, v94
	v_and_b32_e32 v93, 0xffff0000, v94
	global_store_dwordx4 v128, v[104:107], s[8:9] offset:2048
	v_mfma_f32_32x32x16_bf16 v[64:79], v[172:175], v[120:123], v[64:79]
	v_lshlrev_b32_e32 v94, 16, v95
	v_and_b32_e32 v95, 0xffff0000, v95
	global_store_dwordx4 v128, v[108:111], s[8:9] offset:3072
	v_mul_f32_e32 v0, v142, v0
	v_mul_f32_e32 v1, v142, v1
	v_mfma_f32_32x32x16_bf16 v[64:79], v[178:181], v[124:127], v[64:79]
	v_mul_f32_e32 v2, v142, v2
	v_mul_f32_e32 v3, v142, v3
	v_mul_f32_e32 v4, v142, v4
	v_mul_f32_e32 v5, v142, v5
	v_mul_f32_e32 v6, v142, v6
	s_waitcnt lgkmcnt(0)
; DI bf16x8 packS(const f32x16& x, int s) { return pack8(x[8 * s], x[8 * s + 1], x[8 * s + 2], x[8 * s + 3], x[8 * s + 4], x[8 * s + 5], x[8 * s + 6], x[8 * s + 7]); }
; #define SCAN_MMK(F, mh) do { _Pragma("unroll") for (int q = 0; q < 4; ++q) { const int j2 = q >> 1, sx = q & 1; S[2 * (mh)] = MFMA32(F[q], Vb[j2][sx], S[2 * (mh)]); S[2 * (mh) + 1] = MFMA32(F[4 + q], Vb[j2][sx], S[2 * (mh) + 1]); } } while (0)
; DI void gdn_scan_seq(const Params& p, int bh16, char* ldsf) {
;     ...
;     bf16x8 Vb[2][2];
; #pragma unroll
;     for (int j2 = 0; j2 < 2; ++j2) { Vb[j2][0] = packS(vn[j2], 0); Vb[j2][1] = packS(vn[j2], 1); }
; #pragma unroll
;     for (int m = 0; m < 4; ++m)
; #pragma unroll
;       for (int r = 0; r < 16; ++r) S[m][r] *= gl;
;     SCAN_MMK(fa, 0);
;     SCAN_MMK(fb, 1);
;     ...
;     asm volatile("s_waitcnt lgkmcnt(0)" ::: "memory");
;     sl = sl == 2 ? 0 : sl + 1;
;   }
	ds_read_b128 v[148:151], v131 offset:16384
	ds_read_b128 v[152:155], v131 offset:17408
	ds_read_b128 v[156:159], v131 offset:20480
	ds_read_b128 v[160:163], v131 offset:21504
	ds_read_b128 v[164:167], v131 offset:24576
	ds_read_b128 v[168:171], v131 offset:25600
	ds_read_b128 v[172:175], v131 offset:28672
	ds_read_b128 v[178:181], v131 offset:29696
	v_mfma_f32_32x32x16_bf16 v[80:95], v[182:185], v[96:99], v[80:95]
	v_mul_f32_e32 v7, v142, v7
	v_mul_f32_e32 v8, v142, v8
	v_mul_f32_e32 v9, v142, v9
	v_mul_f32_e32 v10, v142, v10
	v_mul_f32_e32 v11, v142, v11
	v_mfma_f32_32x32x16_bf16 v[80:95], v[190:193], v[100:103], v[80:95]
	v_mul_f32_e32 v12, v142, v12
	v_mul_f32_e32 v13, v142, v13
	v_mul_f32_e32 v14, v142, v14
	v_mul_f32_e32 v15, v142, v15
	global_store_dwordx4 v128, v[112:115], s[10:11]
	v_mfma_f32_32x32x16_bf16 v[80:95], v[194:197], v[104:107], v[80:95]
	v_mul_f32_e32 v16, v142, v16
	v_mul_f32_e32 v17, v142, v17
	v_mul_f32_e32 v18, v142, v18
	v_mul_f32_e32 v19, v142, v19
	global_store_dwordx4 v128, v[116:119], s[10:11] offset:1024
	v_mul_f32_e32 v32, v142, v32
	v_mfma_f32_32x32x16_bf16 v[80:95], v[198:201], v[108:111], v[80:95]
	v_mul_f32_e32 v20, v142, v20
	v_mul_f32_e32 v21, v142, v21
	v_mul_f32_e32 v22, v142, v22
	v_mul_f32_e32 v23, v142, v23
	global_store_dwordx4 v128, v[120:123], s[10:11] offset:2048
	v_mul_f32_e32 v33, v142, v33
	v_mfma_f32_32x32x16_bf16 v[80:95], v[202:205], v[112:115], v[80:95]
	v_mul_f32_e32 v24, v142, v24
	v_mul_f32_e32 v25, v142, v25
	v_mul_f32_e32 v26, v142, v26
	v_mul_f32_e32 v27, v142, v27
	global_store_dwordx4 v128, v[124:127], s[10:11] offset:3072
	v_mul_f32_e32 v34, v142, v34
	v_mfma_f32_32x32x16_bf16 v[80:95], v[208:211], v[116:119], v[80:95]
	v_mul_f32_e32 v28, v142, v28
	v_mul_f32_e32 v29, v142, v29
	v_mul_f32_e32 v30, v142, v30
	v_mul_f32_e32 v31, v142, v31
	v_cvt_pk_bf16_f32 v64, v64, v65
	v_mul_f32_e32 v35, v142, v35
	v_mfma_f32_32x32x16_bf16 v[80:95], v[212:215], v[120:123], v[80:95]
	v_cvt_pk_bf16_f32 v65, v66, v67
	v_cvt_pk_bf16_f32 v66, v68, v69
	v_cvt_pk_bf16_f32 v67, v70, v71
	v_cvt_pk_bf16_f32 v68, v72, v73
	v_cvt_pk_bf16_f32 v69, v74, v75
	v_mul_f32_e32 v36, v142, v36
	v_mfma_f32_32x32x16_bf16 v[80:95], v[216:219], v[124:127], v[80:95]
	v_cvt_pk_bf16_f32 v70, v76, v77
	v_cvt_pk_bf16_f32 v71, v78, v79
	v_mul_f32_e32 v37, v142, v37
	v_mul_f32_e32 v38, v142, v38
	v_mul_f32_e32 v39, v142, v39
	v_mul_f32_e32 v40, v142, v40
	s_waitcnt lgkmcnt(0)
	ds_read_b128 v[182:185], v131 offset:18432
	ds_read_b128 v[190:193], v131 offset:19456
	ds_read_b128 v[194:197], v131 offset:22528
	ds_read_b128 v[198:201], v131 offset:23552
	ds_read_b128 v[202:205], v131 offset:26624
	ds_read_b128 v[208:211], v131 offset:27648
	ds_read_b128 v[212:215], v131 offset:30720
	ds_read_b128 v[216:219], v131 offset:31744
	v_mfma_f32_32x32x16_bf16 v[0:15], v[148:151], v[64:67], v[0:15]
	v_mul_f32_e32 v41, v142, v41
	v_mul_f32_e32 v42, v142, v42
	v_mul_f32_e32 v43, v142, v43
	v_mul_f32_e32 v44, v142, v44
	v_mul_f32_e32 v45, v142, v45
	v_mul_f32_e32 v46, v142, v46
	s_add_u32 s2, s2, 1
	s_xor_b32 s3, s3, 0xc000
	s_add_u32 s18, s18, 4
	s_add_u32 s8, s8, 0x8000
	s_addc_u32 s9, s9, 0
	s_add_u32 s10, s10, 0x8000
	s_addc_u32 s11, s11, 0
	v_mfma_f32_32x32x16_bf16 v[0:15], v[152:155], v[68:71], v[0:15]
	v_mul_f32_e32 v47, v142, v47
	v_mul_f32_e32 v48, v142, v48
	v_mul_f32_e32 v49, v142, v49
	v_mul_f32_e32 v50, v142, v50
	v_mul_f32_e32 v51, v142, v51
	v_mul_f32_e32 v52, v142, v52
	v_mfma_f32_32x32x16_bf16 v[16:31], v[156:159], v[64:67], v[16:31]
	v_mul_f32_e32 v53, v142, v53
	v_mul_f32_e32 v54, v142, v54
	v_mul_f32_e32 v55, v142, v55
	v_mul_f32_e32 v56, v142, v56
	v_mul_f32_e32 v57, v142, v57
	v_mul_f32_e32 v58, v142, v58
	v_mfma_f32_32x32x16_bf16 v[16:31], v[160:163], v[68:71], v[16:31]
	v_mul_f32_e32 v59, v142, v59
	v_mul_f32_e32 v60, v142, v60
	v_mul_f32_e32 v61, v142, v61
	v_mul_f32_e32 v62, v142, v62
	v_mul_f32_e32 v63, v142, v63
	v_cvt_pk_bf16_f32 v80, v80, v81
	v_mfma_f32_32x32x16_bf16 v[32:47], v[164:167], v[64:67], v[32:47]
	v_cvt_pk_bf16_f32 v81, v82, v83
	v_cvt_pk_bf16_f32 v82, v84, v85
	v_cvt_pk_bf16_f32 v83, v86, v87
	v_cvt_pk_bf16_f32 v84, v88, v89
	v_cvt_pk_bf16_f32 v85, v90, v91
	v_cvt_pk_bf16_f32 v86, v92, v93
	v_mfma_f32_32x32x16_bf16 v[32:47], v[168:171], v[68:71], v[32:47]
	v_cvt_pk_bf16_f32 v87, v94, v95
	v_mfma_f32_32x32x16_bf16 v[48:63], v[172:175], v[64:67], v[48:63]
	v_mfma_f32_32x32x16_bf16 v[48:63], v[178:181], v[68:71], v[48:63]
	s_cmp_lt_u32 s2, 0x80
	s_waitcnt lgkmcnt(0)
	s_cbranch_scc1 .Lscan_loop
	s_waitcnt vmcnt(0)
	s_barrier
